# MoE GEMM1 gather: the next unit's 4 slot-table loads (a serialized load/vmcnt(0) ladder at the head of the last K iteration) are issued one K iteration earlier into spare VGPRs and retired by the loop
# baseline (speedup 1.0000x reference)
; __device__ __forceinline__ int otid() { int t = threadIdx.x; asm volatile("" : "+v"(t)); return t; }
; template <class Epi, class Sched, bool GATHER, bool LIGHTSKIP = false>
; __device__ __forceinline__ void gemm_phase(LAS unsigned char* lds, LAS unsigned char* xl, const int lda, const int ldb, const int K, const Sched& S, const Epi& E) {
;     ...
;             if constexpr (GATHER) { if (last && has_next) S.offsets(nxt, lda, vn); }
;     __device__ __forceinline__ void offsets(const GUnit& u, int lda, unsigned (&vo)[2][2]) const {
;         const int tid = otid(); int R[2], C[2];
; #pragma unroll
;         for (int i = 0; i < 2; ++i) stage_rc(tid * 16 + i * 8192, R[i], C[i]);
;         const int e = u.pm, j = u.x1 & 0xffff, n = cnt[e]; const int* slot = (const int*)(opaque_uniform(ws) + WS_SLOT);
; #pragma unroll
;         for (int h = 0; h < 2; ++h)
; #pragma unroll
;             for (int i = 0; i < 2; ++i) { const int idx = j * 256 + h * 128 + R[i]; int tok = 0; if (idx < n) tok = slot[(size_t)e * CAP + idx] >> 1;
;                 vo[h][i] = (unsigned)(tok * lda + C[i]) * 2u; }
.LBB0_1339:
	s_cmpk_eq_i32 s38, 0xe00
	s_cselect_b64 s[98:99], -1, 0
	s_and_b64 s[98:99], s[22:23], s[98:99]
	s_andn2_b64 vcc, exec, s[98:99]
	s_cbranch_vccnz .Lm1pf_done
	v_mov_b32_e32 v241, 0
	v_mov_b32_e32 v242, 0
	v_mov_b32_e32 v243, 0
	v_mov_b32_e32 v244, 0
	v_mov_b32_e32 v4, v0
	v_readfirstlane_b32 s8, v198
	v_ashrrev_i32_e32 v2, 31, v4
	v_lshrrev_b32_e32 v2, 26, v2
	v_lshlrev_b32_e32 v134, 4, v4
	v_add_u32_e32 v2, v4, v2
	v_bfe_i32 v4, v4, 27, 1
	v_lshrrev_b32_e32 v4, 22, v4
	v_add_u32_e32 v4, v134, v4
	v_and_b32_e32 v4, 0xfffffc00, v4
	v_sub_u32_e32 v4, v134, v4
	v_lshrrev_b32_e32 v5, 4, v4
	v_bitop3_b32 v136, v5, v4, 32 bitop3:0x6c
	v_ashrrev_i32_e32 v4, 31, v4
	v_lshrrev_b32_e32 v4, 26, v4
	v_add_u32_e32 v4, v136, v4
	v_ashrrev_i32_e32 v137, 6, v4
	v_mov_b32_e32 v4, s56
	v_ashrrev_i32_e32 v2, 6, v2
	ds_read_b32 v140, v4
	v_readfirstlane_b32 s9, v199
	v_lshlrev_b32_e32 v5, 3, v2
	v_and_b32_e32 v5, -16, v5
	s_add_u32 s8, s8, s36
	v_add_u32_e32 v143, v137, v5
	s_addc_u32 s9, s9, s37
	s_add_u32 s8, s8, 0x44a90000
	v_add_u32_e32 v4, s29, v143
	s_addc_u32 s9, s9, 0
	s_waitcnt lgkmcnt(0)
	v_cmp_lt_i32_e32 vcc, v4, v140
	v_mov_b32_e32 v138, 0
	v_ashrrev_i32_e32 v5, 31, v4
	v_mov_b32_e32 v139, 0
	s_and_saveexec_b64 s[40:41], vcc
	s_cbranch_execz .Lm1pf_1
	v_lshl_add_u64 v[144:145], v[4:5], 2, s[8:9]
	global_load_dword v241, v[144:145], off
.Lm1pf_1:
	s_or_b64 exec, exec, s[40:41]
	v_add_u32_e32 v134, 0x2000, v134
	v_ashrrev_i32_e32 v135, 31, v134
	v_lshrrev_b32_e32 v135, 22, v135
	v_add_u32_e32 v135, v134, v135
	v_ashrrev_i32_e32 v141, 10, v135
	v_mul_i32_i24_e32 v135, 0x400, v141
	v_sub_u32_e32 v134, v134, v135
	v_lshrrev_b32_e32 v135, 4, v134
	v_bitop3_b32 v142, v135, v134, 32 bitop3:0x6c
	v_ashrrev_i32_e32 v135, 31, v142
	v_lshrrev_b32_e32 v135, 26, v135
	v_lshlrev_b32_e32 v134, 3, v141
	v_add_u32_e32 v135, v142, v135
	v_and_b32_e32 v134, -16, v134
	v_ashrrev_i32_e32 v144, 6, v135
	v_add_u32_e32 v145, v144, v134
	v_add_u32_e32 v134, s29, v145
	v_cmp_lt_i32_e32 vcc, v134, v140
	v_ashrrev_i32_e32 v135, 31, v134
	s_and_saveexec_b64 s[40:41], vcc
	s_cbranch_execz .Lm1pf_2
	v_lshl_add_u64 v[146:147], v[134:135], 2, s[8:9]
	global_load_dword v242, v[146:147], off
.Lm1pf_2:
	s_or_b64 exec, exec, s[40:41]
	v_add_u32_e32 v143, s17, v143
	v_cmp_lt_i32_e32 vcc, v143, v140
	v_mov_b32_e32 v143, 0
	v_mov_b32_e32 v146, 0
	s_and_saveexec_b64 s[40:41], vcc
	s_cbranch_execz .Lm1pf_3
	v_lshl_add_u64 v[4:5], v[4:5], 2, s[8:9]
	global_load_dword v243, v[4:5], off offset:512
.Lm1pf_3:
	s_or_b64 exec, exec, s[40:41]
	v_add_u32_e32 v4, s17, v145
	v_cmp_lt_i32_e32 vcc, v4, v140
	s_and_saveexec_b64 s[40:41], vcc
	s_cbranch_execz .Lm1pf_4
	v_lshl_add_u64 v[4:5], v[134:135], 2, s[8:9]
	global_load_dword v244, v[4:5], off offset:512

;     __device__ __forceinline__ void offsets(const GUnit& u, int lda, unsigned (&vo)[2][2]) const {
;     ...
;         const int e = u.pm, j = u.x1 & 0xffff, n = cnt[e]; const int* slot = (const int*)(opaque_uniform(ws) + WS_SLOT);
; #pragma unroll
;         for (int h = 0; h < 2; ++h)
; #pragma unroll
;             for (int i = 0; i < 2; ++i) { const int idx = j * 256 + h * 128 + R[i]; int tok = 0; if (idx < n) tok = slot[(size_t)e * CAP + idx] >> 1;
;                 vo[h][i] = (unsigned)(tok * lda + C[i]) * 2u; }
.Lm1pf_done:
	s_cmpk_eq_i32 s38, 0xf00
	s_cselect_b64 s[6:7], -1, 0
	s_and_b64 s[8:9], s[22:23], s[6:7]
	s_andn2_b64 vcc, exec, s[8:9]
	s_cbranch_vccnz .LBB0_1349
	v_mov_b32_e32 v4, v0
	v_readfirstlane_b32 s8, v198
	v_ashrrev_i32_e32 v2, 31, v4
	v_lshrrev_b32_e32 v2, 26, v2
	v_lshlrev_b32_e32 v134, 4, v4
	v_add_u32_e32 v2, v4, v2
	v_bfe_i32 v4, v4, 27, 1
	v_lshrrev_b32_e32 v4, 22, v4
	v_add_u32_e32 v4, v134, v4
	v_and_b32_e32 v4, 0xfffffc00, v4
	v_sub_u32_e32 v4, v134, v4
	v_lshrrev_b32_e32 v5, 4, v4
	v_bitop3_b32 v136, v5, v4, 32 bitop3:0x6c
	v_ashrrev_i32_e32 v4, 31, v4
	v_lshrrev_b32_e32 v4, 26, v4
	v_add_u32_e32 v4, v136, v4
	v_ashrrev_i32_e32 v137, 6, v4
	v_mov_b32_e32 v4, s56
	v_ashrrev_i32_e32 v2, 6, v2
	ds_read_b32 v140, v4
	v_readfirstlane_b32 s9, v199
	v_lshlrev_b32_e32 v5, 3, v2
	v_and_b32_e32 v5, -16, v5
	s_add_u32 s8, s8, s36
	v_add_u32_e32 v143, v137, v5
	s_addc_u32 s9, s9, s37
	s_add_u32 s8, s8, 0x44a90000
	v_add_u32_e32 v4, s29, v143
	s_addc_u32 s9, s9, 0
	s_waitcnt lgkmcnt(0)
	v_cmp_lt_i32_e32 vcc, v4, v140
	v_mov_b32_e32 v138, 0
	v_ashrrev_i32_e32 v5, 31, v4
	v_mov_b32_e32 v139, 0
	s_and_saveexec_b64 s[40:41], vcc
	s_cbranch_execz .LBB0_1342
	v_lshlrev_b32_e32 v135, 10, v241
	v_and_b32_e32 v139, 0xfffff800, v135
.LBB0_1342:
	s_or_b64 exec, exec, s[40:41]
	v_add_u32_e32 v134, 0x2000, v134
	v_ashrrev_i32_e32 v135, 31, v134
	v_lshrrev_b32_e32 v135, 22, v135
	v_add_u32_e32 v135, v134, v135
	v_ashrrev_i32_e32 v141, 10, v135
	v_mul_i32_i24_e32 v135, 0x400, v141
	v_sub_u32_e32 v134, v134, v135
	v_lshrrev_b32_e32 v135, 4, v134
	v_bitop3_b32 v142, v135, v134, 32 bitop3:0x6c
	v_ashrrev_i32_e32 v135, 31, v142
	v_lshrrev_b32_e32 v135, 26, v135
	v_lshlrev_b32_e32 v134, 3, v141
	v_add_u32_e32 v135, v142, v135
	v_and_b32_e32 v134, -16, v134
	v_ashrrev_i32_e32 v144, 6, v135
	v_add_u32_e32 v145, v144, v134
	v_add_u32_e32 v134, s29, v145
	v_cmp_lt_i32_e32 vcc, v134, v140
	v_ashrrev_i32_e32 v135, 31, v134
	s_and_saveexec_b64 s[40:41], vcc
	s_cbranch_execz .LBB0_1344
	v_lshlrev_b32_e32 v138, 10, v242
	v_and_b32_e32 v138, 0xfffff800, v138
.LBB0_1344:
	s_or_b64 exec, exec, s[40:41]
	v_add_u32_e32 v143, s17, v143
	v_cmp_lt_i32_e32 vcc, v143, v140
	v_mov_b32_e32 v143, 0
	v_mov_b32_e32 v146, 0
	s_and_saveexec_b64 s[40:41], vcc
	s_cbranch_execz .LBB0_1346
	v_lshlrev_b32_e32 v4, 10, v243
	v_and_b32_e32 v146, 0xfffff800, v4
.LBB0_1346:
	s_or_b64 exec, exec, s[40:41]
	v_add_u32_e32 v4, s17, v145
	v_cmp_lt_i32_e32 vcc, v4, v140
	s_and_saveexec_b64 s[40:41], vcc
	s_cbranch_execz .LBB0_1348
	v_lshlrev_b32_e32 v4, 10, v244
	v_and_b32_e32 v143, 0xfffff800, v4
